# stack7
# baseline (speedup 1.0000x reference)
_Z7k_spmm1PKiS0_PKfPK15HIP_vector_typeIjLj2EES0_S2_S2_Pfff:
	s_load_dwordx8 s[4:11], s[0:1], 0x18
	v_and_b32_e32 v10, 63, v0
	s_lshl_b32 s2, s2, 4
	v_lshrrev_b32_e32 v0, 5, v0
	v_and_or_b32 v0, v0, 14, s2
	s_nop 0
	v_readfirstlane_b32 s2, v0
	s_ashr_i32 s3, s2, 31
	s_lshl_b64 s[12:13], s[2:3], 8
	s_waitcnt lgkmcnt(0)
	s_add_u32 s4, s4, s12
	s_addc_u32 s5, s5, s13
	s_lshl_b64 s[12:13], s[2:3], 2
	s_add_u32 s6, s6, s12
	v_lshlrev_b32_e32 v0, 3, v10
	s_addc_u32 s7, s7, s13
	s_lshl_b64 s[2:3], s[2:3], 6
	global_load_dwordx2 v[6:7], v0, s[4:5]
	v_or_b32_e32 v0, s2, v10
	v_mov_b32_e32 v1, s3
	v_lshlrev_b64 v[0:1], 2, v[0:1]
	v_lshl_add_u64 v[8:9], s[10:11], 0, v[0:1]
	v_lshl_add_u64 v[0:1], s[8:9], 0, v[0:1]
	global_load_dword v4, v[8:9], off
	global_load_dword v2, v[8:9], off offset:256
	global_load_dword v5, v[0:1], off
	global_load_dword v3, v[0:1], off offset:256
	s_load_dwordx2 s[4:5], s[6:7], 0x0
	v_lshlrev_b32_e32 v0, 2, v10
	s_waitcnt lgkmcnt(0)
	s_cmp_gt_i32 s4, 16
	s_cbranch_scc0 .LBB1_3
	s_cmp_gt_u32 s4, 24
	s_cbranch_scc0 .LBB1_4
	s_mov_b32 s7, 0
	s_waitcnt vmcnt(4)
	v_readlane_b32 s6, v6, 0
	s_lshl_b64 s[8:9], s[6:7], 8
	s_add_u32 s8, s10, s8
	s_addc_u32 s9, s11, s9
	v_readlane_b32 s6, v6, 1
	global_load_dword v1, v0, s[8:9]
	s_lshl_b64 s[8:9], s[6:7], 8
	s_add_u32 s8, s10, s8
	s_addc_u32 s9, s11, s9
	v_readlane_b32 s6, v6, 2
	global_load_dword v9, v0, s[8:9]
	s_lshl_b64 s[8:9], s[6:7], 8
	s_add_u32 s8, s10, s8
	s_addc_u32 s9, s11, s9
	v_readlane_b32 s6, v6, 3
	global_load_dword v10, v0, s[8:9]
	s_lshl_b64 s[8:9], s[6:7], 8
	s_add_u32 s8, s10, s8
	s_addc_u32 s9, s11, s9
	v_readlane_b32 s6, v6, 4
	global_load_dword v11, v0, s[8:9]
	s_lshl_b64 s[8:9], s[6:7], 8
	s_add_u32 s8, s10, s8
	s_addc_u32 s9, s11, s9
	v_readlane_b32 s6, v6, 5
	global_load_dword v12, v0, s[8:9]
	s_lshl_b64 s[8:9], s[6:7], 8
	s_add_u32 s8, s10, s8
	s_addc_u32 s9, s11, s9
	v_readlane_b32 s6, v6, 6
	global_load_dword v13, v0, s[8:9]
	s_lshl_b64 s[8:9], s[6:7], 8
	s_add_u32 s8, s10, s8
	s_addc_u32 s9, s11, s9
	v_readlane_b32 s6, v6, 7
	global_load_dword v14, v0, s[8:9]
	s_lshl_b64 s[8:9], s[6:7], 8
	s_add_u32 s8, s10, s8
	s_addc_u32 s9, s11, s9
	v_readlane_b32 s6, v6, 8
	global_load_dword v15, v0, s[8:9]
	s_lshl_b64 s[8:9], s[6:7], 8
	s_add_u32 s8, s10, s8
	s_addc_u32 s9, s11, s9
	v_readlane_b32 s6, v6, 9
	global_load_dword v16, v0, s[8:9]
	s_lshl_b64 s[8:9], s[6:7], 8
	s_add_u32 s8, s10, s8
	s_addc_u32 s9, s11, s9
	v_readlane_b32 s6, v6, 10
	global_load_dword v17, v0, s[8:9]
	s_lshl_b64 s[8:9], s[6:7], 8
	s_add_u32 s8, s10, s8
	s_addc_u32 s9, s11, s9
	v_readlane_b32 s6, v6, 11
	global_load_dword v18, v0, s[8:9]
	s_lshl_b64 s[8:9], s[6:7], 8
	s_add_u32 s8, s10, s8
	s_addc_u32 s9, s11, s9
	v_readlane_b32 s6, v6, 12
	global_load_dword v19, v0, s[8:9]
	s_lshl_b64 s[8:9], s[6:7], 8
	s_add_u32 s8, s10, s8
	s_addc_u32 s9, s11, s9
	v_readlane_b32 s6, v6, 13
	global_load_dword v20, v0, s[8:9]
	s_lshl_b64 s[8:9], s[6:7], 8
	s_add_u32 s8, s10, s8
	s_addc_u32 s9, s11, s9
	v_readlane_b32 s6, v6, 14
	global_load_dword v21, v0, s[8:9]
	s_lshl_b64 s[8:9], s[6:7], 8
	s_add_u32 s8, s10, s8
	s_addc_u32 s9, s11, s9
	v_readlane_b32 s6, v6, 15
	global_load_dword v22, v0, s[8:9]
	s_lshl_b64 s[8:9], s[6:7], 8
	s_add_u32 s8, s10, s8
	s_addc_u32 s9, s11, s9
	v_readlane_b32 s6, v6, 16
	global_load_dword v23, v0, s[8:9]
	s_lshl_b64 s[8:9], s[6:7], 8
	s_add_u32 s8, s10, s8
	s_addc_u32 s9, s11, s9
	v_readlane_b32 s6, v6, 17
	global_load_dword v24, v0, s[8:9]
	s_lshl_b64 s[8:9], s[6:7], 8
	s_add_u32 s8, s10, s8
	s_addc_u32 s9, s11, s9
	v_readlane_b32 s6, v6, 18
	global_load_dword v25, v0, s[8:9]
	s_lshl_b64 s[8:9], s[6:7], 8
	s_add_u32 s8, s10, s8
	s_addc_u32 s9, s11, s9
	v_readlane_b32 s6, v6, 19
	global_load_dword v26, v0, s[8:9]
	s_lshl_b64 s[8:9], s[6:7], 8
	s_add_u32 s8, s10, s8
	s_addc_u32 s9, s11, s9
	v_readlane_b32 s6, v6, 20
	global_load_dword v27, v0, s[8:9]
	s_lshl_b64 s[8:9], s[6:7], 8
	s_add_u32 s8, s10, s8
	s_addc_u32 s9, s11, s9
	v_readlane_b32 s6, v6, 21
	global_load_dword v28, v0, s[8:9]
	s_lshl_b64 s[8:9], s[6:7], 8
	s_add_u32 s8, s10, s8
	s_addc_u32 s9, s11, s9
	v_readlane_b32 s6, v6, 22
	global_load_dword v29, v0, s[8:9]
	s_lshl_b64 s[8:9], s[6:7], 8
	s_add_u32 s8, s10, s8
	s_addc_u32 s9, s11, s9
	v_readlane_b32 s6, v6, 23
	global_load_dword v30, v0, s[8:9]
	s_lshl_b64 s[8:9], s[6:7], 8
	s_add_u32 s8, s10, s8
	s_addc_u32 s9, s11, s9
	v_readlane_b32 s6, v6, 24
	global_load_dword v31, v0, s[8:9]
	s_lshl_b64 s[8:9], s[6:7], 8
	s_add_u32 s8, s10, s8
	s_addc_u32 s9, s11, s9
	v_readlane_b32 s6, v6, 25
	global_load_dword v32, v0, s[8:9]
	s_lshl_b64 s[8:9], s[6:7], 8
	s_add_u32 s8, s10, s8
	s_addc_u32 s9, s11, s9
	v_readlane_b32 s6, v6, 26
	global_load_dword v33, v0, s[8:9]
	s_lshl_b64 s[8:9], s[6:7], 8
	s_add_u32 s8, s10, s8
	s_addc_u32 s9, s11, s9
	v_readlane_b32 s6, v6, 27
	global_load_dword v34, v0, s[8:9]
	s_lshl_b64 s[8:9], s[6:7], 8
	s_add_u32 s8, s10, s8
	s_addc_u32 s9, s11, s9
	v_readlane_b32 s6, v6, 28
	global_load_dword v35, v0, s[8:9]
	s_lshl_b64 s[8:9], s[6:7], 8
	s_add_u32 s8, s10, s8
	s_addc_u32 s9, s11, s9
	v_readlane_b32 s6, v6, 29
	global_load_dword v36, v0, s[8:9]
	s_lshl_b64 s[8:9], s[6:7], 8
	s_add_u32 s8, s10, s8
	s_addc_u32 s9, s11, s9
	v_readlane_b32 s6, v6, 30
	global_load_dword v37, v0, s[8:9]
	s_lshl_b64 s[8:9], s[6:7], 8
	s_add_u32 s8, s10, s8
	v_readlane_b32 s6, v6, 31
	s_addc_u32 s9, s11, s9
	s_lshl_b64 s[6:7], s[6:7], 8
	s_add_u32 s6, s10, s6
	v_readlane_b32 s4, v7, 0
	global_load_dword v38, v0, s[8:9]
	s_addc_u32 s7, s11, s7
	global_load_dword v39, v0, s[6:7]
	s_waitcnt vmcnt(0)
	s_nop 0
	v_fma_f32 v8, s4, v1, 0
	v_readlane_b32 s4, v7, 1
	s_nop 1
	v_fmac_f32_e32 v8, s4, v9
	v_readlane_b32 s20, v7, 2
	v_readlane_b32 s21, v7, 3
	v_readlane_b32 s22, v7, 4
	v_readlane_b32 s23, v7, 5
	v_fmac_f32_e32 v8, s20, v10
	v_fmac_f32_e32 v8, s21, v11
	v_fmac_f32_e32 v8, s22, v12
	v_fmac_f32_e32 v8, s23, v13
	v_readlane_b32 s20, v7, 6
	v_readlane_b32 s21, v7, 7
	v_readlane_b32 s22, v7, 8
	v_readlane_b32 s23, v7, 9
	v_fmac_f32_e32 v8, s20, v14
	v_fmac_f32_e32 v8, s21, v15
	v_fmac_f32_e32 v8, s22, v16
	v_fmac_f32_e32 v8, s23, v17
	v_readlane_b32 s20, v7, 10
	v_readlane_b32 s21, v7, 11
	v_readlane_b32 s22, v7, 12
	v_readlane_b32 s23, v7, 13
	v_fmac_f32_e32 v8, s20, v18
	v_fmac_f32_e32 v8, s21, v19
	v_fmac_f32_e32 v8, s22, v20
	v_fmac_f32_e32 v8, s23, v21
	v_readlane_b32 s20, v7, 14
	v_readlane_b32 s21, v7, 15
	v_readlane_b32 s22, v7, 16
	v_readlane_b32 s23, v7, 17
	v_fmac_f32_e32 v8, s20, v22
	v_fmac_f32_e32 v8, s21, v23
	v_fmac_f32_e32 v8, s22, v24
	v_fmac_f32_e32 v8, s23, v25
	v_readlane_b32 s20, v7, 18
	v_readlane_b32 s21, v7, 19
	v_readlane_b32 s22, v7, 20
	v_readlane_b32 s23, v7, 21
	v_fmac_f32_e32 v8, s20, v26
	v_fmac_f32_e32 v8, s21, v27
	v_fmac_f32_e32 v8, s22, v28
	v_fmac_f32_e32 v8, s23, v29
	v_readlane_b32 s20, v7, 22
	v_readlane_b32 s21, v7, 23
	v_readlane_b32 s22, v7, 24
	v_readlane_b32 s23, v7, 25
	v_fmac_f32_e32 v8, s20, v30
	v_fmac_f32_e32 v8, s21, v31
	v_fmac_f32_e32 v8, s22, v32
	v_fmac_f32_e32 v8, s23, v33
	v_readlane_b32 s20, v7, 26
	v_readlane_b32 s21, v7, 27
	v_readlane_b32 s22, v7, 28
	v_readlane_b32 s23, v7, 29
	v_fmac_f32_e32 v8, s20, v34
	v_fmac_f32_e32 v8, s21, v35
	v_fmac_f32_e32 v8, s22, v36
	v_fmac_f32_e32 v8, s23, v37
	v_readlane_b32 s20, v7, 30
	s_nop 1
	v_fmac_f32_e32 v8, s20, v38
	v_readlane_b32 s20, v7, 31
	s_nop 1
	v_fmac_f32_e32 v8, s20, v39
	s_cbranch_execz .LBB1_5
	s_branch .LBB1_6

.LBB1_4:
.LBB1_5:
	s_mov_b32 s7, 0
	s_waitcnt vmcnt(4)
	v_readlane_b32 s6, v6, 0
	s_lshl_b64 s[8:9], s[6:7], 8
	s_add_u32 s8, s10, s8
	s_addc_u32 s9, s11, s9
	v_readlane_b32 s6, v6, 1
	global_load_dword v1, v0, s[8:9]
	s_lshl_b64 s[8:9], s[6:7], 8
	s_add_u32 s8, s10, s8
	s_addc_u32 s9, s11, s9
	v_readlane_b32 s6, v6, 2
	global_load_dword v9, v0, s[8:9]
	s_lshl_b64 s[8:9], s[6:7], 8
	s_add_u32 s8, s10, s8
	s_addc_u32 s9, s11, s9
	v_readlane_b32 s6, v6, 3
	global_load_dword v10, v0, s[8:9]
	s_lshl_b64 s[8:9], s[6:7], 8
	s_add_u32 s8, s10, s8
	s_addc_u32 s9, s11, s9
	v_readlane_b32 s6, v6, 4
	global_load_dword v11, v0, s[8:9]
	s_lshl_b64 s[8:9], s[6:7], 8
	s_add_u32 s8, s10, s8
	s_addc_u32 s9, s11, s9
	v_readlane_b32 s6, v6, 5
	global_load_dword v12, v0, s[8:9]
	s_lshl_b64 s[8:9], s[6:7], 8
	s_add_u32 s8, s10, s8
	s_addc_u32 s9, s11, s9
	v_readlane_b32 s6, v6, 6
	global_load_dword v13, v0, s[8:9]
	s_lshl_b64 s[8:9], s[6:7], 8
	s_add_u32 s8, s10, s8
	s_addc_u32 s9, s11, s9
	v_readlane_b32 s6, v6, 7
	global_load_dword v14, v0, s[8:9]
	s_lshl_b64 s[8:9], s[6:7], 8
	s_add_u32 s8, s10, s8
	s_addc_u32 s9, s11, s9
	v_readlane_b32 s6, v6, 8
	global_load_dword v15, v0, s[8:9]
	s_lshl_b64 s[8:9], s[6:7], 8
	s_add_u32 s8, s10, s8
	s_addc_u32 s9, s11, s9
	v_readlane_b32 s6, v6, 9
	global_load_dword v16, v0, s[8:9]
	s_lshl_b64 s[8:9], s[6:7], 8
	s_add_u32 s8, s10, s8
	s_addc_u32 s9, s11, s9
	v_readlane_b32 s6, v6, 10
	global_load_dword v17, v0, s[8:9]
	s_lshl_b64 s[8:9], s[6:7], 8
	s_add_u32 s8, s10, s8
	s_addc_u32 s9, s11, s9
	v_readlane_b32 s6, v6, 11
	global_load_dword v18, v0, s[8:9]
	s_lshl_b64 s[8:9], s[6:7], 8
	s_add_u32 s8, s10, s8
	s_addc_u32 s9, s11, s9
	v_readlane_b32 s6, v6, 12
	global_load_dword v19, v0, s[8:9]
	s_lshl_b64 s[8:9], s[6:7], 8
	s_add_u32 s8, s10, s8
	s_addc_u32 s9, s11, s9
	v_readlane_b32 s6, v6, 13
	global_load_dword v20, v0, s[8:9]
	s_lshl_b64 s[8:9], s[6:7], 8
	s_add_u32 s8, s10, s8
	s_addc_u32 s9, s11, s9
	v_readlane_b32 s6, v6, 14
	global_load_dword v21, v0, s[8:9]
	s_lshl_b64 s[8:9], s[6:7], 8
	s_add_u32 s8, s10, s8
	s_addc_u32 s9, s11, s9
	v_readlane_b32 s6, v6, 15
	global_load_dword v22, v0, s[8:9]
	s_lshl_b64 s[8:9], s[6:7], 8
	s_add_u32 s8, s10, s8
	s_addc_u32 s9, s11, s9
	v_readlane_b32 s6, v6, 16
	global_load_dword v23, v0, s[8:9]
	s_lshl_b64 s[8:9], s[6:7], 8
	s_add_u32 s8, s10, s8
	s_addc_u32 s9, s11, s9
	v_readlane_b32 s6, v6, 17
	global_load_dword v24, v0, s[8:9]
	s_lshl_b64 s[8:9], s[6:7], 8
	s_add_u32 s8, s10, s8
	s_addc_u32 s9, s11, s9
	v_readlane_b32 s6, v6, 18
	global_load_dword v25, v0, s[8:9]
	s_lshl_b64 s[8:9], s[6:7], 8
	s_add_u32 s8, s10, s8
	s_addc_u32 s9, s11, s9
	v_readlane_b32 s6, v6, 19
	global_load_dword v26, v0, s[8:9]
	s_lshl_b64 s[8:9], s[6:7], 8
	s_add_u32 s8, s10, s8
	s_addc_u32 s9, s11, s9
	v_readlane_b32 s6, v6, 20
	global_load_dword v27, v0, s[8:9]
	s_lshl_b64 s[8:9], s[6:7], 8
	s_add_u32 s8, s10, s8
	s_addc_u32 s9, s11, s9
	v_readlane_b32 s6, v6, 21
	global_load_dword v28, v0, s[8:9]
	s_lshl_b64 s[8:9], s[6:7], 8
	s_add_u32 s8, s10, s8
	s_addc_u32 s9, s11, s9
	v_readlane_b32 s6, v6, 22
	global_load_dword v29, v0, s[8:9]
	s_lshl_b64 s[8:9], s[6:7], 8
	s_add_u32 s8, s10, s8
	v_readlane_b32 s6, v6, 23
	s_addc_u32 s9, s11, s9
	s_lshl_b64 s[6:7], s[6:7], 8
	s_add_u32 s6, s10, s6
	v_readlane_b32 s4, v7, 0
	global_load_dword v30, v0, s[8:9]
	s_addc_u32 s7, s11, s7
	global_load_dword v31, v0, s[6:7]
	s_waitcnt vmcnt(0)
	s_nop 0
	v_fma_f32 v8, s4, v1, 0
	v_readlane_b32 s4, v7, 1
	s_nop 1
	v_fmac_f32_e32 v8, s4, v9
	v_readlane_b32 s20, v7, 2
	v_readlane_b32 s21, v7, 3
	v_readlane_b32 s22, v7, 4
	v_readlane_b32 s23, v7, 5
	v_fmac_f32_e32 v8, s20, v10
	v_fmac_f32_e32 v8, s21, v11
	v_fmac_f32_e32 v8, s22, v12
	v_fmac_f32_e32 v8, s23, v13
	v_readlane_b32 s20, v7, 6
	v_readlane_b32 s21, v7, 7
	v_readlane_b32 s22, v7, 8
	v_readlane_b32 s23, v7, 9
	v_fmac_f32_e32 v8, s20, v14
	v_fmac_f32_e32 v8, s21, v15
	v_fmac_f32_e32 v8, s22, v16
	v_fmac_f32_e32 v8, s23, v17
	v_readlane_b32 s20, v7, 10
	v_readlane_b32 s21, v7, 11
	v_readlane_b32 s22, v7, 12
	v_readlane_b32 s23, v7, 13
	v_fmac_f32_e32 v8, s20, v18
	v_fmac_f32_e32 v8, s21, v19
	v_fmac_f32_e32 v8, s22, v20
	v_fmac_f32_e32 v8, s23, v21
	v_readlane_b32 s20, v7, 14
	v_readlane_b32 s21, v7, 15
	v_readlane_b32 s22, v7, 16
	v_readlane_b32 s23, v7, 17
	v_fmac_f32_e32 v8, s20, v22
	v_fmac_f32_e32 v8, s21, v23
	v_fmac_f32_e32 v8, s22, v24
	v_fmac_f32_e32 v8, s23, v25
	v_readlane_b32 s20, v7, 18
	v_readlane_b32 s21, v7, 19
	v_readlane_b32 s22, v7, 20
	v_readlane_b32 s23, v7, 21
	v_fmac_f32_e32 v8, s20, v26
	v_fmac_f32_e32 v8, s21, v27
	v_fmac_f32_e32 v8, s22, v28
	v_fmac_f32_e32 v8, s23, v29
	v_readlane_b32 s20, v7, 22
	s_nop 1
	v_fmac_f32_e32 v8, s20, v30
	v_readlane_b32 s20, v7, 23
	s_nop 1
	v_fmac_f32_e32 v8, s20, v31

.LBB1_7:
	s_mov_b32 s7, 0
	s_waitcnt vmcnt(4)
	v_readlane_b32 s6, v6, 0
	s_lshl_b64 s[8:9], s[6:7], 8
	s_add_u32 s8, s10, s8
	s_addc_u32 s9, s11, s9
	v_readlane_b32 s6, v6, 1
	global_load_dword v1, v0, s[8:9]
	s_lshl_b64 s[8:9], s[6:7], 8
	s_add_u32 s8, s10, s8
	s_addc_u32 s9, s11, s9
	v_readlane_b32 s6, v6, 2
	global_load_dword v9, v0, s[8:9]
	s_lshl_b64 s[8:9], s[6:7], 8
	s_add_u32 s8, s10, s8
	s_addc_u32 s9, s11, s9
	v_readlane_b32 s6, v6, 3
	global_load_dword v10, v0, s[8:9]
	s_lshl_b64 s[8:9], s[6:7], 8
	s_add_u32 s8, s10, s8
	s_addc_u32 s9, s11, s9
	v_readlane_b32 s6, v6, 4
	global_load_dword v11, v0, s[8:9]
	s_lshl_b64 s[8:9], s[6:7], 8
	s_add_u32 s8, s10, s8
	s_addc_u32 s9, s11, s9
	v_readlane_b32 s6, v6, 5
	global_load_dword v12, v0, s[8:9]
	s_lshl_b64 s[8:9], s[6:7], 8
	s_add_u32 s8, s10, s8
	s_addc_u32 s9, s11, s9
	v_readlane_b32 s6, v6, 6
	global_load_dword v13, v0, s[8:9]
	s_lshl_b64 s[8:9], s[6:7], 8
	s_add_u32 s8, s10, s8
	s_addc_u32 s9, s11, s9
	v_readlane_b32 s6, v6, 7
	global_load_dword v14, v0, s[8:9]
	s_lshl_b64 s[8:9], s[6:7], 8
	s_add_u32 s8, s10, s8
	s_addc_u32 s9, s11, s9
	v_readlane_b32 s6, v6, 8
	global_load_dword v15, v0, s[8:9]
	s_lshl_b64 s[8:9], s[6:7], 8
	s_add_u32 s8, s10, s8
	s_addc_u32 s9, s11, s9
	v_readlane_b32 s6, v6, 9
	global_load_dword v16, v0, s[8:9]
	s_lshl_b64 s[8:9], s[6:7], 8
	s_add_u32 s8, s10, s8
	s_addc_u32 s9, s11, s9
	v_readlane_b32 s6, v6, 10
	global_load_dword v17, v0, s[8:9]
	s_lshl_b64 s[8:9], s[6:7], 8
	s_add_u32 s8, s10, s8
	s_addc_u32 s9, s11, s9
	v_readlane_b32 s6, v6, 11
	global_load_dword v18, v0, s[8:9]
	s_lshl_b64 s[8:9], s[6:7], 8
	s_add_u32 s8, s10, s8
	s_addc_u32 s9, s11, s9
	v_readlane_b32 s6, v6, 12
	global_load_dword v19, v0, s[8:9]
	s_lshl_b64 s[8:9], s[6:7], 8
	s_add_u32 s8, s10, s8
	s_addc_u32 s9, s11, s9
	v_readlane_b32 s6, v6, 13
	global_load_dword v20, v0, s[8:9]
	s_lshl_b64 s[8:9], s[6:7], 8
	s_add_u32 s8, s10, s8
	s_addc_u32 s9, s11, s9
	v_readlane_b32 s6, v6, 14
	global_load_dword v21, v0, s[8:9]
	s_lshl_b64 s[8:9], s[6:7], 8
	s_add_u32 s8, s10, s8
	v_readlane_b32 s6, v6, 15
	s_addc_u32 s9, s11, s9
	s_lshl_b64 s[6:7], s[6:7], 8
	s_add_u32 s6, s10, s6
	v_readlane_b32 s4, v7, 0
	global_load_dword v22, v0, s[8:9]
	s_addc_u32 s7, s11, s7
	global_load_dword v23, v0, s[6:7]
	s_waitcnt vmcnt(0)
	s_nop 0
	v_fma_f32 v8, s4, v1, 0
	v_readlane_b32 s4, v7, 1
	s_nop 1
	v_fmac_f32_e32 v8, s4, v9
	v_readlane_b32 s20, v7, 2
	v_readlane_b32 s21, v7, 3
	v_readlane_b32 s22, v7, 4
	v_readlane_b32 s23, v7, 5
	v_fmac_f32_e32 v8, s20, v10
	v_fmac_f32_e32 v8, s21, v11
	v_fmac_f32_e32 v8, s22, v12
	v_fmac_f32_e32 v8, s23, v13
	v_readlane_b32 s20, v7, 6
	v_readlane_b32 s21, v7, 7
	v_readlane_b32 s22, v7, 8
	v_readlane_b32 s23, v7, 9
	v_fmac_f32_e32 v8, s20, v14
	v_fmac_f32_e32 v8, s21, v15
	v_fmac_f32_e32 v8, s22, v16
	v_fmac_f32_e32 v8, s23, v17
	v_readlane_b32 s20, v7, 10
	v_readlane_b32 s21, v7, 11
	v_readlane_b32 s22, v7, 12
	v_readlane_b32 s23, v7, 13
	v_fmac_f32_e32 v8, s20, v18
	v_fmac_f32_e32 v8, s21, v19
	v_fmac_f32_e32 v8, s22, v20
	v_fmac_f32_e32 v8, s23, v21
	v_readlane_b32 s20, v7, 14
	s_nop 1
	v_fmac_f32_e32 v8, s20, v22
	v_readlane_b32 s20, v7, 15
	s_nop 1
	v_fmac_f32_e32 v8, s20, v23
.LBB1_8:
	s_load_dwordx2 s[8:9], s[0:1], 0x0
	s_cmp_gt_i32 s5, 16
	s_cbranch_scc0 .LBB1_11
	s_cmp_gt_u32 s5, 24
	s_cbranch_scc0 .LBB1_12
	s_waitcnt vmcnt(4)
	v_readlane_b32 s4, v6, 32
	s_mov_b32 s5, 0
	s_lshl_b64 s[6:7], s[4:5], 8
	s_add_u32 s6, s10, s6
	s_addc_u32 s7, s11, s7
	v_readlane_b32 s4, v6, 33
	global_load_dword v1, v0, s[6:7]
	s_lshl_b64 s[6:7], s[4:5], 8
	s_add_u32 s6, s10, s6
	s_addc_u32 s7, s11, s7
	v_readlane_b32 s4, v6, 34
	global_load_dword v10, v0, s[6:7]
	s_lshl_b64 s[6:7], s[4:5], 8
	s_add_u32 s6, s10, s6
	s_addc_u32 s7, s11, s7
	v_readlane_b32 s4, v6, 35
	global_load_dword v11, v0, s[6:7]
	s_lshl_b64 s[6:7], s[4:5], 8
	s_add_u32 s6, s10, s6
	s_addc_u32 s7, s11, s7
	v_readlane_b32 s4, v6, 36
	global_load_dword v12, v0, s[6:7]
	s_lshl_b64 s[6:7], s[4:5], 8
	s_add_u32 s6, s10, s6
	s_addc_u32 s7, s11, s7
	v_readlane_b32 s4, v6, 37
	global_load_dword v13, v0, s[6:7]
	s_lshl_b64 s[6:7], s[4:5], 8
	s_add_u32 s6, s10, s6
	s_addc_u32 s7, s11, s7
	v_readlane_b32 s4, v6, 38
	global_load_dword v14, v0, s[6:7]
	s_lshl_b64 s[6:7], s[4:5], 8
	s_add_u32 s6, s10, s6
	s_addc_u32 s7, s11, s7
	v_readlane_b32 s4, v6, 39
	global_load_dword v15, v0, s[6:7]
	s_lshl_b64 s[6:7], s[4:5], 8
	s_add_u32 s6, s10, s6
	s_addc_u32 s7, s11, s7
	v_readlane_b32 s4, v6, 40
	global_load_dword v16, v0, s[6:7]
	s_lshl_b64 s[6:7], s[4:5], 8
	s_add_u32 s6, s10, s6
	s_addc_u32 s7, s11, s7
	v_readlane_b32 s4, v6, 41
	global_load_dword v17, v0, s[6:7]
	s_lshl_b64 s[6:7], s[4:5], 8
	s_add_u32 s6, s10, s6
	s_addc_u32 s7, s11, s7
	v_readlane_b32 s4, v6, 42
	global_load_dword v18, v0, s[6:7]
	s_lshl_b64 s[6:7], s[4:5], 8
	s_add_u32 s6, s10, s6
	s_addc_u32 s7, s11, s7
	v_readlane_b32 s4, v6, 43
	global_load_dword v19, v0, s[6:7]
	s_lshl_b64 s[6:7], s[4:5], 8
	s_add_u32 s6, s10, s6
	s_addc_u32 s7, s11, s7
	v_readlane_b32 s4, v6, 44
	global_load_dword v20, v0, s[6:7]
	s_lshl_b64 s[6:7], s[4:5], 8
	s_add_u32 s6, s10, s6
	s_addc_u32 s7, s11, s7
	v_readlane_b32 s4, v6, 45
	global_load_dword v21, v0, s[6:7]
	s_lshl_b64 s[6:7], s[4:5], 8
	s_add_u32 s6, s10, s6
	s_addc_u32 s7, s11, s7
	v_readlane_b32 s4, v6, 46
	global_load_dword v22, v0, s[6:7]
	s_lshl_b64 s[6:7], s[4:5], 8
	s_add_u32 s6, s10, s6
	s_addc_u32 s7, s11, s7
	v_readlane_b32 s4, v6, 47
	global_load_dword v23, v0, s[6:7]
	s_lshl_b64 s[6:7], s[4:5], 8
	s_add_u32 s6, s10, s6
	s_addc_u32 s7, s11, s7
	v_readlane_b32 s4, v6, 48
	global_load_dword v24, v0, s[6:7]
	s_lshl_b64 s[6:7], s[4:5], 8
	s_add_u32 s6, s10, s6
	s_addc_u32 s7, s11, s7
	v_readlane_b32 s4, v6, 49
	global_load_dword v25, v0, s[6:7]
	s_lshl_b64 s[6:7], s[4:5], 8
	s_add_u32 s6, s10, s6
	s_addc_u32 s7, s11, s7
	v_readlane_b32 s4, v6, 50
	global_load_dword v26, v0, s[6:7]
	s_lshl_b64 s[6:7], s[4:5], 8
	s_add_u32 s6, s10, s6
	s_addc_u32 s7, s11, s7
	v_readlane_b32 s4, v6, 51
	global_load_dword v27, v0, s[6:7]
	s_lshl_b64 s[6:7], s[4:5], 8
	s_add_u32 s6, s10, s6
	s_addc_u32 s7, s11, s7
	v_readlane_b32 s4, v6, 52
	global_load_dword v28, v0, s[6:7]
	s_lshl_b64 s[6:7], s[4:5], 8
	s_add_u32 s6, s10, s6
	s_addc_u32 s7, s11, s7
	v_readlane_b32 s4, v6, 53
	global_load_dword v29, v0, s[6:7]
	s_lshl_b64 s[6:7], s[4:5], 8
	s_add_u32 s6, s10, s6
	s_addc_u32 s7, s11, s7
	v_readlane_b32 s4, v6, 54
	global_load_dword v30, v0, s[6:7]
	s_lshl_b64 s[6:7], s[4:5], 8
	s_add_u32 s6, s10, s6
	s_addc_u32 s7, s11, s7
	v_readlane_b32 s4, v6, 55
	global_load_dword v31, v0, s[6:7]
	s_lshl_b64 s[6:7], s[4:5], 8
	s_add_u32 s6, s10, s6
	s_addc_u32 s7, s11, s7
	v_readlane_b32 s4, v6, 56
	global_load_dword v32, v0, s[6:7]
	s_lshl_b64 s[6:7], s[4:5], 8
	s_add_u32 s6, s10, s6
	s_addc_u32 s7, s11, s7
	v_readlane_b32 s4, v6, 57
	global_load_dword v33, v0, s[6:7]
	s_lshl_b64 s[6:7], s[4:5], 8
	s_add_u32 s6, s10, s6
	s_addc_u32 s7, s11, s7
	v_readlane_b32 s4, v6, 58
	global_load_dword v34, v0, s[6:7]
	s_lshl_b64 s[6:7], s[4:5], 8
	s_add_u32 s6, s10, s6
	s_addc_u32 s7, s11, s7
	v_readlane_b32 s4, v6, 59
	global_load_dword v35, v0, s[6:7]
	s_lshl_b64 s[6:7], s[4:5], 8
	s_add_u32 s6, s10, s6
	s_addc_u32 s7, s11, s7
	v_readlane_b32 s4, v6, 60
	global_load_dword v36, v0, s[6:7]
	s_lshl_b64 s[6:7], s[4:5], 8
	s_add_u32 s6, s10, s6
	s_addc_u32 s7, s11, s7
	v_readlane_b32 s4, v6, 61
	global_load_dword v37, v0, s[6:7]
	s_lshl_b64 s[6:7], s[4:5], 8
	s_add_u32 s6, s10, s6
	s_addc_u32 s7, s11, s7
	v_readlane_b32 s4, v6, 62
	global_load_dword v38, v0, s[6:7]
	s_lshl_b64 s[6:7], s[4:5], 8
	s_add_u32 s6, s10, s6
	v_readlane_b32 s4, v6, 63
	s_addc_u32 s7, s11, s7
	s_lshl_b64 s[4:5], s[4:5], 8
	s_add_u32 s4, s10, s4
	global_load_dword v39, v0, s[6:7]
	s_addc_u32 s5, s11, s5
	global_load_dword v40, v0, s[4:5]
	v_readlane_b32 s4, v7, 32
	s_waitcnt vmcnt(0)
	s_nop 1
	v_fma_f32 v9, s4, v1, 0
	v_readlane_b32 s20, v7, 33
	v_readlane_b32 s21, v7, 34
	v_readlane_b32 s22, v7, 35
	v_readlane_b32 s23, v7, 36
	v_fmac_f32_e32 v9, s20, v10
	v_fmac_f32_e32 v9, s21, v11
	v_fmac_f32_e32 v9, s22, v12
	v_fmac_f32_e32 v9, s23, v13
	v_readlane_b32 s20, v7, 37
	v_readlane_b32 s21, v7, 38
	v_readlane_b32 s22, v7, 39
	v_readlane_b32 s23, v7, 40
	v_fmac_f32_e32 v9, s20, v14
	v_fmac_f32_e32 v9, s21, v15
	v_fmac_f32_e32 v9, s22, v16
	v_fmac_f32_e32 v9, s23, v17
	v_readlane_b32 s20, v7, 41
	v_readlane_b32 s21, v7, 42
	v_readlane_b32 s22, v7, 43
	v_readlane_b32 s23, v7, 44
	v_fmac_f32_e32 v9, s20, v18
	v_fmac_f32_e32 v9, s21, v19
	v_fmac_f32_e32 v9, s22, v20
	v_fmac_f32_e32 v9, s23, v21
	v_readlane_b32 s20, v7, 45
	v_readlane_b32 s21, v7, 46
	v_readlane_b32 s22, v7, 47
	v_readlane_b32 s23, v7, 48
	v_fmac_f32_e32 v9, s20, v22
	v_fmac_f32_e32 v9, s21, v23
	v_fmac_f32_e32 v9, s22, v24
	v_fmac_f32_e32 v9, s23, v25
	v_readlane_b32 s20, v7, 49
	v_readlane_b32 s21, v7, 50
	v_readlane_b32 s22, v7, 51
	v_readlane_b32 s23, v7, 52
	v_fmac_f32_e32 v9, s20, v26
	v_fmac_f32_e32 v9, s21, v27
	v_fmac_f32_e32 v9, s22, v28
	v_fmac_f32_e32 v9, s23, v29
	v_readlane_b32 s20, v7, 53
	v_readlane_b32 s21, v7, 54
	v_readlane_b32 s22, v7, 55
	v_readlane_b32 s23, v7, 56
	v_fmac_f32_e32 v9, s20, v30
	v_fmac_f32_e32 v9, s21, v31
	v_fmac_f32_e32 v9, s22, v32
	v_fmac_f32_e32 v9, s23, v33
	v_readlane_b32 s20, v7, 57
	v_readlane_b32 s21, v7, 58
	v_readlane_b32 s22, v7, 59
	v_readlane_b32 s23, v7, 60
	v_fmac_f32_e32 v9, s20, v34
	v_fmac_f32_e32 v9, s21, v35
	v_fmac_f32_e32 v9, s22, v36
	v_fmac_f32_e32 v9, s23, v37
	v_readlane_b32 s20, v7, 61
	v_readlane_b32 s21, v7, 62
	v_readlane_b32 s22, v7, 63
	v_fmac_f32_e32 v9, s20, v38
	v_fmac_f32_e32 v9, s21, v39
	v_fmac_f32_e32 v9, s22, v40
	s_cbranch_execz .LBB1_13
	s_branch .LBB1_14

.LBB1_12:
.LBB1_13:
	s_waitcnt vmcnt(4)
	v_readlane_b32 s4, v6, 32
	s_mov_b32 s5, 0
	s_lshl_b64 s[6:7], s[4:5], 8
	s_add_u32 s6, s10, s6
	s_addc_u32 s7, s11, s7
	v_readlane_b32 s4, v6, 33
	global_load_dword v1, v0, s[6:7]
	s_lshl_b64 s[6:7], s[4:5], 8
	s_add_u32 s6, s10, s6
	s_addc_u32 s7, s11, s7
	v_readlane_b32 s4, v6, 34
	global_load_dword v10, v0, s[6:7]
	s_lshl_b64 s[6:7], s[4:5], 8
	s_add_u32 s6, s10, s6
	s_addc_u32 s7, s11, s7
	v_readlane_b32 s4, v6, 35
	global_load_dword v11, v0, s[6:7]
	s_lshl_b64 s[6:7], s[4:5], 8
	s_add_u32 s6, s10, s6
	s_addc_u32 s7, s11, s7
	v_readlane_b32 s4, v6, 36
	global_load_dword v12, v0, s[6:7]
	s_lshl_b64 s[6:7], s[4:5], 8
	s_add_u32 s6, s10, s6
	s_addc_u32 s7, s11, s7
	v_readlane_b32 s4, v6, 37
	global_load_dword v13, v0, s[6:7]
	s_lshl_b64 s[6:7], s[4:5], 8
	s_add_u32 s6, s10, s6
	s_addc_u32 s7, s11, s7
	v_readlane_b32 s4, v6, 38
	global_load_dword v14, v0, s[6:7]
	s_lshl_b64 s[6:7], s[4:5], 8
	s_add_u32 s6, s10, s6
	s_addc_u32 s7, s11, s7
	v_readlane_b32 s4, v6, 39
	global_load_dword v15, v0, s[6:7]
	s_lshl_b64 s[6:7], s[4:5], 8
	s_add_u32 s6, s10, s6
	s_addc_u32 s7, s11, s7
	v_readlane_b32 s4, v6, 40
	global_load_dword v16, v0, s[6:7]
	s_lshl_b64 s[6:7], s[4:5], 8
	s_add_u32 s6, s10, s6
	s_addc_u32 s7, s11, s7
	v_readlane_b32 s4, v6, 41
	global_load_dword v17, v0, s[6:7]
	s_lshl_b64 s[6:7], s[4:5], 8
	s_add_u32 s6, s10, s6
	s_addc_u32 s7, s11, s7
	v_readlane_b32 s4, v6, 42
	global_load_dword v18, v0, s[6:7]
	s_lshl_b64 s[6:7], s[4:5], 8
	s_add_u32 s6, s10, s6
	s_addc_u32 s7, s11, s7
	v_readlane_b32 s4, v6, 43
	global_load_dword v19, v0, s[6:7]
	s_lshl_b64 s[6:7], s[4:5], 8
	s_add_u32 s6, s10, s6
	s_addc_u32 s7, s11, s7
	v_readlane_b32 s4, v6, 44
	global_load_dword v20, v0, s[6:7]
	s_lshl_b64 s[6:7], s[4:5], 8
	s_add_u32 s6, s10, s6
	s_addc_u32 s7, s11, s7
	v_readlane_b32 s4, v6, 45
	global_load_dword v21, v0, s[6:7]
	s_lshl_b64 s[6:7], s[4:5], 8
	s_add_u32 s6, s10, s6
	s_addc_u32 s7, s11, s7
	v_readlane_b32 s4, v6, 46
	global_load_dword v22, v0, s[6:7]
	s_lshl_b64 s[6:7], s[4:5], 8
	s_add_u32 s6, s10, s6
	s_addc_u32 s7, s11, s7
	v_readlane_b32 s4, v6, 47
	global_load_dword v23, v0, s[6:7]
	s_lshl_b64 s[6:7], s[4:5], 8
	s_add_u32 s6, s10, s6
	s_addc_u32 s7, s11, s7
	v_readlane_b32 s4, v6, 48
	global_load_dword v24, v0, s[6:7]
	s_lshl_b64 s[6:7], s[4:5], 8
	s_add_u32 s6, s10, s6
	s_addc_u32 s7, s11, s7
	v_readlane_b32 s4, v6, 49
	global_load_dword v25, v0, s[6:7]
	s_lshl_b64 s[6:7], s[4:5], 8
	s_add_u32 s6, s10, s6
	s_addc_u32 s7, s11, s7
	v_readlane_b32 s4, v6, 50
	global_load_dword v26, v0, s[6:7]
	s_lshl_b64 s[6:7], s[4:5], 8
	s_add_u32 s6, s10, s6
	s_addc_u32 s7, s11, s7
	v_readlane_b32 s4, v6, 51
	global_load_dword v27, v0, s[6:7]
	s_lshl_b64 s[6:7], s[4:5], 8
	s_add_u32 s6, s10, s6
	s_addc_u32 s7, s11, s7
	v_readlane_b32 s4, v6, 52
	global_load_dword v28, v0, s[6:7]
	s_lshl_b64 s[6:7], s[4:5], 8
	s_add_u32 s6, s10, s6
	s_addc_u32 s7, s11, s7
	v_readlane_b32 s4, v6, 53
	global_load_dword v29, v0, s[6:7]
	s_lshl_b64 s[6:7], s[4:5], 8
	s_add_u32 s6, s10, s6
	s_addc_u32 s7, s11, s7
	v_readlane_b32 s4, v6, 54
	global_load_dword v30, v0, s[6:7]
	s_lshl_b64 s[6:7], s[4:5], 8
	s_add_u32 s6, s10, s6
	v_readlane_b32 s4, v6, 55
	s_addc_u32 s7, s11, s7
	s_lshl_b64 s[4:5], s[4:5], 8
	s_add_u32 s4, s10, s4
	global_load_dword v31, v0, s[6:7]
	s_addc_u32 s5, s11, s5
	global_load_dword v32, v0, s[4:5]
	v_readlane_b32 s4, v7, 32
	s_waitcnt vmcnt(0)
	s_nop 1
	v_fma_f32 v9, s4, v1, 0
	v_readlane_b32 s20, v7, 33
	v_readlane_b32 s21, v7, 34
	v_readlane_b32 s22, v7, 35
	v_readlane_b32 s23, v7, 36
	v_fmac_f32_e32 v9, s20, v10
	v_fmac_f32_e32 v9, s21, v11
	v_fmac_f32_e32 v9, s22, v12
	v_fmac_f32_e32 v9, s23, v13
	v_readlane_b32 s20, v7, 37
	v_readlane_b32 s21, v7, 38
	v_readlane_b32 s22, v7, 39
	v_readlane_b32 s23, v7, 40
	v_fmac_f32_e32 v9, s20, v14
	v_fmac_f32_e32 v9, s21, v15
	v_fmac_f32_e32 v9, s22, v16
	v_fmac_f32_e32 v9, s23, v17
	v_readlane_b32 s20, v7, 41
	v_readlane_b32 s21, v7, 42
	v_readlane_b32 s22, v7, 43
	v_readlane_b32 s23, v7, 44
	v_fmac_f32_e32 v9, s20, v18
	v_fmac_f32_e32 v9, s21, v19
	v_fmac_f32_e32 v9, s22, v20
	v_fmac_f32_e32 v9, s23, v21
	v_readlane_b32 s20, v7, 45
	v_readlane_b32 s21, v7, 46
	v_readlane_b32 s22, v7, 47
	v_readlane_b32 s23, v7, 48
	v_fmac_f32_e32 v9, s20, v22
	v_fmac_f32_e32 v9, s21, v23
	v_fmac_f32_e32 v9, s22, v24
	v_fmac_f32_e32 v9, s23, v25
	v_readlane_b32 s20, v7, 49
	v_readlane_b32 s21, v7, 50
	v_readlane_b32 s22, v7, 51
	v_readlane_b32 s23, v7, 52
	v_fmac_f32_e32 v9, s20, v26
	v_fmac_f32_e32 v9, s21, v27
	v_fmac_f32_e32 v9, s22, v28
	v_fmac_f32_e32 v9, s23, v29
	v_readlane_b32 s20, v7, 53
	v_readlane_b32 s21, v7, 54
	v_readlane_b32 s22, v7, 55
	v_fmac_f32_e32 v9, s20, v30
	v_fmac_f32_e32 v9, s21, v31
	v_fmac_f32_e32 v9, s22, v32

.LBB1_15:
	s_waitcnt vmcnt(4)
	v_readlane_b32 s14, v6, 32
	s_mov_b32 s15, 0
	s_lshl_b64 s[16:17], s[14:15], 8
	s_add_u32 s16, s10, s16
	s_addc_u32 s17, s11, s17
	v_readlane_b32 s14, v6, 33
	global_load_dword v1, v0, s[16:17]
	s_lshl_b64 s[16:17], s[14:15], 8
	s_add_u32 s16, s10, s16
	s_addc_u32 s17, s11, s17
	v_readlane_b32 s14, v6, 34
	global_load_dword v10, v0, s[16:17]
	s_lshl_b64 s[16:17], s[14:15], 8
	s_add_u32 s16, s10, s16
	s_addc_u32 s17, s11, s17
	v_readlane_b32 s14, v6, 35
	global_load_dword v11, v0, s[16:17]
	s_lshl_b64 s[16:17], s[14:15], 8
	s_add_u32 s16, s10, s16
	s_addc_u32 s17, s11, s17
	v_readlane_b32 s14, v6, 36
	global_load_dword v12, v0, s[16:17]
	s_lshl_b64 s[16:17], s[14:15], 8
	s_add_u32 s16, s10, s16
	s_addc_u32 s17, s11, s17
	v_readlane_b32 s14, v6, 37
	global_load_dword v13, v0, s[16:17]
	s_lshl_b64 s[16:17], s[14:15], 8
	s_add_u32 s16, s10, s16
	s_addc_u32 s17, s11, s17
	v_readlane_b32 s14, v6, 38
	global_load_dword v14, v0, s[16:17]
	s_lshl_b64 s[16:17], s[14:15], 8
	s_add_u32 s16, s10, s16
	s_addc_u32 s17, s11, s17
	v_readlane_b32 s14, v6, 39
	global_load_dword v15, v0, s[16:17]
	s_lshl_b64 s[16:17], s[14:15], 8
	s_add_u32 s16, s10, s16
	s_addc_u32 s17, s11, s17
	v_readlane_b32 s14, v6, 40
	global_load_dword v16, v0, s[16:17]
	s_lshl_b64 s[16:17], s[14:15], 8
	s_add_u32 s16, s10, s16
	s_addc_u32 s17, s11, s17
	v_readlane_b32 s14, v6, 41
	global_load_dword v17, v0, s[16:17]
	s_lshl_b64 s[16:17], s[14:15], 8
	s_add_u32 s16, s10, s16
	s_addc_u32 s17, s11, s17
	v_readlane_b32 s14, v6, 42
	global_load_dword v18, v0, s[16:17]
	s_lshl_b64 s[16:17], s[14:15], 8
	s_add_u32 s16, s10, s16
	s_addc_u32 s17, s11, s17
	v_readlane_b32 s14, v6, 43
	global_load_dword v19, v0, s[16:17]
	s_lshl_b64 s[16:17], s[14:15], 8
	s_add_u32 s16, s10, s16
	s_addc_u32 s17, s11, s17
	v_readlane_b32 s14, v6, 44
	global_load_dword v20, v0, s[16:17]
	s_lshl_b64 s[16:17], s[14:15], 8
	s_add_u32 s16, s10, s16
	s_addc_u32 s17, s11, s17
	v_readlane_b32 s14, v6, 45
	global_load_dword v21, v0, s[16:17]
	s_lshl_b64 s[16:17], s[14:15], 8
	s_add_u32 s16, s10, s16
	s_addc_u32 s17, s11, s17
	v_readlane_b32 s14, v6, 46
	global_load_dword v22, v0, s[16:17]
	s_lshl_b64 s[16:17], s[14:15], 8
	s_add_u32 s16, s10, s16
	v_readlane_b32 s14, v6, 47
	s_addc_u32 s17, s11, s17
	s_lshl_b64 s[14:15], s[14:15], 8
	s_add_u32 s14, s10, s14
	global_load_dword v23, v0, s[16:17]
	s_addc_u32 s15, s11, s15
	global_load_dword v6, v0, s[14:15]
	v_readlane_b32 s14, v7, 32
	s_waitcnt vmcnt(0)
	s_nop 1
	v_fma_f32 v9, s14, v1, 0
	v_readlane_b32 s20, v7, 33
	v_readlane_b32 s21, v7, 34
	v_readlane_b32 s22, v7, 35
	v_readlane_b32 s23, v7, 36
	v_fmac_f32_e32 v9, s20, v10
	v_fmac_f32_e32 v9, s21, v11
	v_fmac_f32_e32 v9, s22, v12
	v_fmac_f32_e32 v9, s23, v13
	v_readlane_b32 s20, v7, 37
	v_readlane_b32 s21, v7, 38
	v_readlane_b32 s22, v7, 39
	v_readlane_b32 s23, v7, 40
	v_fmac_f32_e32 v9, s20, v14
	v_fmac_f32_e32 v9, s21, v15
	v_fmac_f32_e32 v9, s22, v16
	v_fmac_f32_e32 v9, s23, v17
	v_readlane_b32 s20, v7, 41
	v_readlane_b32 s21, v7, 42
	v_readlane_b32 s22, v7, 43
	v_readlane_b32 s23, v7, 44
	v_fmac_f32_e32 v9, s20, v18
	v_fmac_f32_e32 v9, s21, v19
	v_fmac_f32_e32 v9, s22, v20
	v_fmac_f32_e32 v9, s23, v21
	v_readlane_b32 s20, v7, 45
	v_readlane_b32 s21, v7, 46
	v_readlane_b32 s22, v7, 47
	v_fmac_f32_e32 v9, s20, v22
	v_fmac_f32_e32 v9, s21, v23
	v_fmac_f32_e32 v9, s22, v6

	.amdhsa_kernel _Z7k_spmm1PKiS0_PKfPK15HIP_vector_typeIjLj2EES0_S2_S2_Pfff
		.amdhsa_group_segment_fixed_size 0
		.amdhsa_private_segment_fixed_size 0
		.amdhsa_kernarg_size 72
		.amdhsa_user_sgpr_count 2
		.amdhsa_user_sgpr_dispatch_ptr 0
		.amdhsa_user_sgpr_queue_ptr 0
		.amdhsa_user_sgpr_kernarg_segment_ptr 1
		.amdhsa_user_sgpr_dispatch_id 0
		.amdhsa_user_sgpr_kernarg_preload_length 0
		.amdhsa_user_sgpr_kernarg_preload_offset 0
		.amdhsa_user_sgpr_private_segment_size 0
		.amdhsa_uses_dynamic_stack 0
		.amdhsa_enable_private_segment 0
		.amdhsa_system_sgpr_workgroup_id_x 1
		.amdhsa_system_sgpr_workgroup_id_y 0
		.amdhsa_system_sgpr_workgroup_id_z 0
		.amdhsa_system_sgpr_workgroup_info 0
		.amdhsa_system_vgpr_workitem_id 0
		.amdhsa_next_free_vgpr 41
		.amdhsa_next_free_sgpr 24
		.amdhsa_accum_offset 44
		.amdhsa_reserve_vcc 0
		.amdhsa_float_round_mode_32 0
		.amdhsa_float_round_mode_16_64 0
		.amdhsa_float_denorm_mode_32 3
		.amdhsa_float_denorm_mode_16_64 3
		.amdhsa_dx10_clamp 1
		.amdhsa_ieee_mode 1
		.amdhsa_fp16_overflow 0
		.amdhsa_tg_split 0
		.amdhsa_exception_fp_ieee_invalid_op 0
		.amdhsa_exception_fp_denorm_src 0
		.amdhsa_exception_fp_ieee_div_zero 0
		.amdhsa_exception_fp_ieee_overflow 0
		.amdhsa_exception_fp_ieee_underflow 0
		.amdhsa_exception_fp_ieee_inexact 0
		.amdhsa_exception_int_div_zero 0
	.end_amdhsa_kernel

amdhsa.kernels:
  - .agpr_count:     0
    .args:
      - .actual_access:  read_only
        .address_space:  global
        .offset:         0
        .size:           8
        .value_kind:     global_buffer
      - .actual_access:  read_only
        .address_space:  global
        .offset:         8
        .size:           8
        .value_kind:     global_buffer
      - .actual_access:  write_only
        .address_space:  global
        .offset:         16
        .size:           8
        .value_kind:     global_buffer
      - .actual_access:  write_only
        .address_space:  global
        .offset:         24
        .size:           8
        .value_kind:     global_buffer
      - .actual_access:  write_only
        .address_space:  global
        .offset:         32
        .size:           8
        .value_kind:     global_buffer
      - .actual_access:  read_only
        .address_space:  global
        .offset:         40
        .size:           8
        .value_kind:     global_buffer
    .group_segment_fixed_size: 1024
    .kernarg_segment_align: 8
    .kernarg_segment_size: 48
    .language:       OpenCL C
    .language_version:
      - 2
      - 0
    .max_flat_workgroup_size: 1024
    .name:           _Z7k_sort2PKiPKfPiS3_S3_Pf
    .private_segment_fixed_size: 0
    .sgpr_count:     18
    .sgpr_spill_count: 0
    .symbol:         _Z7k_sort2PKiPKfPiS3_S3_Pf.kd
    .uniform_work_group_size: 1
    .uses_dynamic_stack: false
    .vgpr_count:     25
    .vgpr_spill_count: 0
    .wavefront_size: 64
  - .agpr_count:     0
    .args:
      - .actual_access:  read_only
        .address_space:  global
        .offset:         0
        .size:           8
        .value_kind:     global_buffer
      - .actual_access:  read_only
        .address_space:  global
        .offset:         8
        .size:           8
        .value_kind:     global_buffer
      - .actual_access:  read_only
        .address_space:  global
        .offset:         16
        .size:           8
        .value_kind:     global_buffer
      - .actual_access:  read_only
        .address_space:  global
        .offset:         24
        .size:           8
        .value_kind:     global_buffer
      - .actual_access:  read_only
        .address_space:  global
        .offset:         32
        .size:           8
        .value_kind:     global_buffer
      - .actual_access:  read_only
        .address_space:  global
        .offset:         40
        .size:           8
        .value_kind:     global_buffer
      - .address_space:  global
        .offset:         48
        .size:           8
        .value_kind:     global_buffer
      - .address_space:  global
        .offset:         56
        .size:           8
        .value_kind:     global_buffer
      - .offset:         64
        .size:           4
        .value_kind:     by_value
      - .offset:         68
        .size:           4
        .value_kind:     by_value
    .group_segment_fixed_size: 0
    .kernarg_segment_align: 8
    .kernarg_segment_size: 72
    .language:       OpenCL C
    .language_version:
      - 2
      - 0
    .max_flat_workgroup_size: 512
    .name:           _Z7k_spmm1PKiS0_PKfPK15HIP_vector_typeIjLj2EES0_S2_S2_Pfff
    .private_segment_fixed_size: 0
    .sgpr_count:     30
    .sgpr_spill_count: 0
    .symbol:         _Z7k_spmm1PKiS0_PKfPK15HIP_vector_typeIjLj2EES0_S2_S2_Pfff.kd
    .uniform_work_group_size: 1
    .uses_dynamic_stack: false
    .vgpr_count:     41
    .vgpr_spill_count: 0
    .wavefront_size: 64
  - .agpr_count:     0
    .args:
      - .address_space:  global
        .offset:         0
        .size:           8
        .value_kind:     global_buffer
      - .actual_access:  read_only
        .address_space:  global
        .offset:         8
        .size:           8
        .value_kind:     global_buffer
      - .actual_access:  read_only
        .address_space:  global
        .offset:         16
        .size:           8
        .value_kind:     global_buffer
      - .actual_access:  write_only
        .address_space:  global
        .offset:         24
        .size:           8
        .value_kind:     global_buffer
    .group_segment_fixed_size: 32768
    .kernarg_segment_align: 8
    .kernarg_segment_size: 32
    .language:       OpenCL C
    .language_version:
      - 2
      - 0
    .max_flat_workgroup_size: 512
    .name:           _Z7k_conv1PKfS0_S0_Pf
    .private_segment_fixed_size: 0
    .sgpr_count:     46
    .sgpr_spill_count: 0
    .symbol:         _Z7k_conv1PKfS0_S0_Pf.kd
    .uniform_work_group_size: 1
    .uses_dynamic_stack: false
    .vgpr_count:     107
    .vgpr_spill_count: 0
    .wavefront_size: 64
  - .agpr_count:     0
    .args:
      - .actual_access:  read_only
        .address_space:  global
        .offset:         0
        .size:           8
        .value_kind:     global_buffer
      - .actual_access:  read_only
        .address_space:  global
        .offset:         8
        .size:           8
        .value_kind:     global_buffer
      - .actual_access:  read_only
        .address_space:  global
        .offset:         16
        .size:           8
        .value_kind:     global_buffer
      - .address_space:  global
        .offset:         24
        .size:           8
        .value_kind:     global_buffer
      - .actual_access:  read_only
        .address_space:  global
        .offset:         32
        .size:           8
        .value_kind:     global_buffer
      - .actual_access:  read_only
        .address_space:  global
        .offset:         40
        .size:           8
        .value_kind:     global_buffer
      - .actual_access:  write_only
        .address_space:  global
        .offset:         48
        .size:           8
        .value_kind:     global_buffer
      - .actual_access:  write_only
        .address_space:  global
        .offset:         56
        .size:           8
        .value_kind:     global_buffer
      - .actual_access:  write_only
        .address_space:  global
        .offset:         64
        .size:           8
        .value_kind:     global_buffer
    .group_segment_fixed_size: 139392
    .kernarg_segment_align: 8
    .kernarg_segment_size: 72
    .language:       OpenCL C
    .language_version:
      - 2
      - 0
    .max_flat_workgroup_size: 512
    .name:           _Z6k_rec2PKiS0_S0_PK15HIP_vector_typeIjLj4EEPKfS6_PS2_PS1_IjLj2EEPf
    .private_segment_fixed_size: 0
    .sgpr_count:     75
    .sgpr_spill_count: 0
    .symbol:         _Z6k_rec2PKiS0_S0_PK15HIP_vector_typeIjLj4EEPKfS6_PS2_PS1_IjLj2EEPf.kd
    .uniform_work_group_size: 1
    .uses_dynamic_stack: false
    .vgpr_count:     246
    .vgpr_spill_count: 0
    .wavefront_size: 64
  - .agpr_count:     0
    .args:
      - .address_space:  global
        .offset:         0
        .size:           8
        .value_kind:     global_buffer
      - .address_space:  global
        .offset:         8
        .size:           8
        .value_kind:     global_buffer
      - .actual_access:  read_only
        .address_space:  global
        .offset:         16
        .size:           8
        .value_kind:     global_buffer
      - .actual_access:  read_only
        .address_space:  global
        .offset:         24
        .size:           8
        .value_kind:     global_buffer
      - .actual_access:  read_only
        .address_space:  global
        .offset:         32
        .size:           8
        .value_kind:     global_buffer
      - .actual_access:  read_only
        .address_space:  global
        .offset:         40
        .size:           8
        .value_kind:     global_buffer
      - .actual_access:  write_only
        .address_space:  global
        .offset:         48
        .size:           8
        .value_kind:     global_buffer
      - .actual_access:  write_only
        .address_space:  global
        .offset:         56
        .size:           8
        .value_kind:     global_buffer
    .group_segment_fixed_size: 127376
    .kernarg_segment_align: 8
    .kernarg_segment_size: 64
    .language:       OpenCL C
    .language_version:
      - 2
      - 0
    .max_flat_workgroup_size: 1024
    .name:           _Z7k_gemm2PK15HIP_vector_typeIjLj4EEPKS_IjLj2EEPKfS2_S2_S7_PtS8_
    .private_segment_fixed_size: 0
    .sgpr_count:     26
    .sgpr_spill_count: 0
    .symbol:         _Z7k_gemm2PK15HIP_vector_typeIjLj4EEPKS_IjLj2EEPKfS2_S2_S7_PtS8_.kd
    .uniform_work_group_size: 1
    .uses_dynamic_stack: false
    .vgpr_count:     115
    .vgpr_spill_count: 0
    .wavefront_size: 64
  - .agpr_count:     32
    .args:
      - .address_space:  global
        .offset:         0
        .size:           8
        .value_kind:     global_buffer
      - .address_space:  global
        .offset:         8
        .size:           8
        .value_kind:     global_buffer
      - .address_space:  global
        .offset:         16
        .size:           8
        .value_kind:     global_buffer
      - .actual_access:  write_only
        .address_space:  global
        .offset:         24
        .size:           8
        .value_kind:     global_buffer
    .group_segment_fixed_size: 65536
    .kernarg_segment_align: 8
    .kernarg_segment_size: 32
    .language:       OpenCL C
    .language_version:
      - 2
      - 0
    .max_flat_workgroup_size: 256
    .name:           _Z5k_fc1PKtS0_PKfPf
    .private_segment_fixed_size: 0
    .sgpr_count:     49
    .sgpr_spill_count: 0
    .symbol:         _Z5k_fc1PKtS0_PKfPf.kd
    .uniform_work_group_size: 1
    .uses_dynamic_stack: false
    .vgpr_count:     172
    .vgpr_spill_count: 0
    .wavefront_size: 64
  - .agpr_count:     0
    .args:
      - .actual_access:  read_only
        .address_space:  global
        .offset:         0
        .size:           8
        .value_kind:     global_buffer
      - .actual_access:  read_only
        .address_space:  global
        .offset:         8
        .size:           8
        .value_kind:     global_buffer
      - .actual_access:  read_only
        .address_space:  global
        .offset:         16
        .size:           8
        .value_kind:     global_buffer
      - .actual_access:  read_only
        .address_space:  global
        .offset:         24
        .size:           8
        .value_kind:     global_buffer
      - .actual_access:  write_only
        .address_space:  global
        .offset:         32
        .size:           8
        .value_kind:     global_buffer
    .group_segment_fixed_size: 2048
    .kernarg_segment_align: 8
    .kernarg_segment_size: 40
    .language:       OpenCL C
    .language_version:
      - 2
      - 0
    .max_flat_workgroup_size: 512
    .name:           _Z5k_fc2PKfS0_S0_S0_Pf
    .private_segment_fixed_size: 0
    .sgpr_count:     18
    .sgpr_spill_count: 0
    .symbol:         _Z5k_fc2PKfS0_S0_S0_Pf.kd
    .uniform_work_group_size: 1
    .uses_dynamic_stack: false
    .vgpr_count:     96
    .vgpr_spill_count: 0
    .wavefront_size: 64
  - .agpr_count:     0
    .args:
      - .actual_access:  read_only
        .address_space:  global
        .offset:         0
        .size:           8
        .value_kind:     global_buffer
      - .actual_access:  read_only
        .address_space:  global
        .offset:         8
        .size:           8
        .value_kind:     global_buffer
      - .actual_access:  read_only
        .address_space:  global
        .offset:         16
        .size:           8
        .value_kind:     global_buffer
      - .actual_access:  read_only
        .address_space:  global
        .offset:         24
        .size:           8
        .value_kind:     global_buffer
      - .actual_access:  write_only
        .address_space:  global
        .offset:         32
        .size:           8
        .value_kind:     global_buffer
      - .actual_access:  write_only
        .address_space:  global
        .offset:         40
        .size:           8
        .value_kind:     global_buffer
      - .actual_access:  write_only
        .address_space:  global
        .offset:         48
        .size:           8
        .value_kind:     global_buffer
      - .actual_access:  write_only
        .address_space:  global
        .offset:         56
        .size:           8
        .value_kind:     global_buffer
      - .actual_access:  write_only
        .address_space:  global
        .offset:         64
        .size:           8
        .value_kind:     global_buffer
    .group_segment_fixed_size: 16640
    .kernarg_segment_align: 8
    .kernarg_segment_size: 72
    .language:       OpenCL C
    .language_version:
      - 2
      - 0
    .max_flat_workgroup_size: 256
    .name:           _Z7k_prepAPKiS0_PKfS2_PiS3_PtS4_Pf
    .private_segment_fixed_size: 0
    .sgpr_count:     20
    .sgpr_spill_count: 0
    .symbol:         _Z7k_prepAPKiS0_PKfS2_PiS3_PtS4_Pf.kd
    .uniform_work_group_size: 1
    .uses_dynamic_stack: false
    .vgpr_count:     24
    .vgpr_spill_count: 0
    .wavefront_size: 64
  - .agpr_count:     0
    .args:
      - .actual_access:  read_only
        .address_space:  global
        .offset:         0
        .size:           8
        .value_kind:     global_buffer
      - .actual_access:  read_only
        .address_space:  global
        .offset:         8
        .size:           8
        .value_kind:     global_buffer
      - .actual_access:  read_only
        .address_space:  global
        .offset:         16
        .size:           8
        .value_kind:     global_buffer
      - .actual_access:  write_only
        .address_space:  global
        .offset:         24
        .size:           8
        .value_kind:     global_buffer
      - .actual_access:  write_only
        .address_space:  global
        .offset:         32
        .size:           8
        .value_kind:     global_buffer
      - .actual_access:  read_only
        .address_space:  global
        .offset:         40
        .size:           8
        .value_kind:     global_buffer
      - .actual_access:  read_only
        .address_space:  global
        .offset:         48
        .size:           8
        .value_kind:     global_buffer
      - .actual_access:  read_only
        .address_space:  global
        .offset:         56
        .size:           8
        .value_kind:     global_buffer
      - .actual_access:  read_only
        .address_space:  global
        .offset:         64
        .size:           8
        .value_kind:     global_buffer
      - .actual_access:  read_only
        .address_space:  global
        .offset:         72
        .size:           8
        .value_kind:     global_buffer
      - .actual_access:  read_only
        .address_space:  global
        .offset:         80
        .size:           8
        .value_kind:     global_buffer
      - .actual_access:  read_only
        .address_space:  global
        .offset:         88
        .size:           8
        .value_kind:     global_buffer
      - .actual_access:  write_only
        .address_space:  global
        .offset:         96
        .size:           8
        .value_kind:     global_buffer
    .group_segment_fixed_size: 0
    .kernarg_segment_align: 8
    .kernarg_segment_size: 104
    .language:       OpenCL C
    .language_version:
      - 2
      - 0
    .max_flat_workgroup_size: 256
    .name:           _Z7k_prepBPKiS0_PKfP15HIP_vector_typeIjLj2EEPiS0_S0_S2_S0_S0_S0_S2_Pj
    .private_segment_fixed_size: 0
    .sgpr_count:     21
    .sgpr_spill_count: 0
    .symbol:         _Z7k_prepBPKiS0_PKfP15HIP_vector_typeIjLj2EEPiS0_S0_S2_S0_S0_S0_S2_Pj.kd
    .uniform_work_group_size: 1
    .uses_dynamic_stack: false
    .vgpr_count:     14
    .vgpr_spill_count: 0
    .wavefront_size: 64
